# MLA loop re-interleaved at even VALU cost per MFMA (exp in place, LDS fragments in a 4-quad FIFO); DIFF and GQA loops as in the previous version
# speedup vs baseline: 1.0034x; 1.0034x over previous
.LBB0_926:
	v_lshlrev_b32_e32 v12, 10, v4
	v_and_b32_e32 v4, 19, v3
	v_lshlrev_b32_e32 v5, 1, v2
	v_lshrrev_b32_e32 v3, 1, v3
	s_add_u32 s12, s30, s25
	v_and_b32_e32 v5, 8, v5
	v_and_b32_e32 v3, 4, v3
	s_addc_u32 s13, s31, s26
	v_or3_b32 v3, v4, v5, v3
	v_lshl_add_u64 v[4:5], s[12:13], 0, v[0:1]
	v_lshl_add_u64 v[4:5], v[4:5], 0, s[52:53]
	s_add_i32 m0, s27, 0x8000
	v_lshl_or_b32 v231, v3, 4, v12
	global_load_lds_dwordx4 v[4:5], off
	v_mov_b32_e32 v178, v1
	v_add_u32_e32 v232, 0, v231
	s_waitcnt vmcnt(0)
	s_waitcnt vmcnt(0) lgkmcnt(0)
	s_barrier
	ds_read_b128 v[4:7], v232
	ds_read_b128 v[98:101], v232 offset:512
	s_waitcnt lgkmcnt(1)
	v_mfma_f32_32x32x16_bf16 v[82:97], v[4:7], v[130:133], 0
	v_lshl_or_b32 v233, v2, 4, v12
	v_mov_b32_e32 v2, 0
	s_mov_b32 s12, 1
	s_mov_b32 s33, 0
	v_add_u32_e32 v234, 0, v233
	s_mov_b32 s13, 2
	s_mov_b32 s30, 0
	v_mfma_f32_32x32x16_bf16 v[66:81], v[4:7], v[170:173], 0
	ds_read_b128 v[4:7], v232 offset:2048
	ds_read_b128 v[194:197], v232 offset:2560
	ds_read_b128 v[8:11], v232 offset:4096
	ds_read_b128 v[12:15], v232 offset:6144
	ds_read_b128 v[18:21], v232 offset:8192
	ds_read_b128 v[22:25], v232 offset:10240
	s_mov_b32 s31, 0
	v_mov_b32_e32 v179, v178
	v_mov_b32_e32 v180, v178
	v_mov_b32_e32 v181, v178
	s_waitcnt lgkmcnt(5)
	v_mfma_f32_32x32x16_bf16 v[82:97], v[4:7], v[134:137], v[82:97]
	v_mov_b32_e32 v182, v178
	v_mov_b32_e32 v183, v178
	v_mov_b32_e32 v184, v178
	v_mov_b32_e32 v185, v178
	v_mov_b32_e32 v190, v178
	v_mov_b32_e32 v191, v178
	v_mov_b32_e32 v192, v178
	v_mfma_f32_32x32x16_bf16 v[66:81], v[4:7], v[138:141], v[66:81]
	v_mov_b32_e32 v193, v178
	v_mov_b32_e32 v186, v178
	v_mov_b32_e32 v187, v178
	v_mov_b32_e32 v188, v178
	v_mov_b32_e32 v189, v178
	v_mov_b32_e32 v3, v2
	v_mov_b32_e32 v4, v2
	s_waitcnt lgkmcnt(3)
	v_mfma_f32_32x32x16_bf16 v[82:97], v[8:11], v[146:149], v[82:97]
	v_mov_b32_e32 v5, v2
	v_mov_b32_e32 v6, v2
	v_mov_b32_e32 v7, v2
	v_mov_b32_e32 v16, v2
	v_mov_b32_e32 v17, v2
	v_mov_b32_e32 v50, v2
	v_mov_b32_e32 v51, v2
	v_mfma_f32_32x32x16_bf16 v[66:81], v[8:11], v[142:145], v[66:81]
	v_mov_b32_e32 v8, v2
	v_mov_b32_e32 v9, v2
	v_mov_b32_e32 v10, v2
	v_mov_b32_e32 v11, v2
	v_mov_b32_e32 v52, v2
	v_mov_b32_e32 v53, v2
	v_mov_b32_e32 v54, v2
	s_waitcnt lgkmcnt(2)
	v_mfma_f32_32x32x16_bf16 v[82:97], v[12:15], v[150:153], v[82:97]
	v_mov_b32_e32 v55, v2
	v_mov_b32_e32 v56, v2
	v_mov_b32_e32 v57, v2
	v_mov_b32_e32 v58, v2
	v_mov_b32_e32 v59, v2
	v_mov_b32_e32 v60, v2
	v_mov_b32_e32 v61, v2
	v_mfma_f32_32x32x16_bf16 v[66:81], v[12:15], v[154:157], v[66:81]
	v_mov_b32_e32 v12, v2
	v_mov_b32_e32 v13, v2
	v_mov_b32_e32 v14, v2
	v_mov_b32_e32 v15, v2
	v_mov_b32_e32 v62, v2
	v_mov_b32_e32 v63, v2
	v_mov_b32_e32 v64, v2
	s_waitcnt lgkmcnt(1)
	v_mfma_f32_32x32x16_bf16 v[82:97], v[18:21], v[162:165], v[82:97]
	v_mov_b32_e32 v65, v2
	v_mov_b32_e32 v34, v2
	v_mov_b32_e32 v35, v2
	v_mov_b32_e32 v36, v2
	v_mov_b32_e32 v37, v2
	v_mov_b32_e32 v38, v2
	v_mov_b32_e32 v39, v2
	v_mfma_f32_32x32x16_bf16 v[66:81], v[18:21], v[158:161], v[66:81]
	v_mov_b32_e32 v40, v2
	v_mov_b32_e32 v41, v2
	v_mov_b32_e32 v42, v2
	v_mov_b32_e32 v43, v2
	v_mov_b32_e32 v44, v2
	v_mov_b32_e32 v45, v2
	v_mov_b32_e32 v46, v2
	s_waitcnt lgkmcnt(0)
	v_mfma_f32_32x32x16_bf16 v[82:97], v[22:25], v[166:169], v[82:97]
	v_mov_b32_e32 v47, v2
	v_mov_b32_e32 v48, v2
	v_mov_b32_e32 v49, v2
	v_mov_b32_e32 v18, v2
	v_mov_b32_e32 v19, v2
	v_mov_b32_e32 v20, v2
	v_mov_b32_e32 v21, v2
	v_mfma_f32_32x32x16_bf16 v[66:81], v[22:25], v[174:177], v[66:81]
	v_mov_b32_e32 v22, v2
	v_mov_b32_e32 v23, v2
	v_mov_b32_e32 v24, v2
	v_mov_b32_e32 v25, v2
	v_mov_b32_e32 v26, v2
	v_mov_b32_e32 v27, v2
	v_mov_b32_e32 v28, v2
	v_mov_b32_e32 v29, v2
	v_mov_b32_e32 v30, v2
	v_mov_b32_e32 v31, v2
	v_mov_b32_e32 v32, v2
	v_mov_b32_e32 v33, v2
	v_mov_b32_e32 v202, v2
	v_mov_b32_e32 v203, v2
	v_mov_b32_e32 v212, v202
	v_mov_b32_e32 v213, v203
	s_waitcnt lgkmcnt(0)
	v_mov_b32_e32 v240, v98
	v_mov_b32_e32 v241, v99
	v_mov_b32_e32 v242, v100
	v_mov_b32_e32 v243, v101
	v_mov_b32_e32 v244, v194
	v_mov_b32_e32 v245, v195
	v_mov_b32_e32 v246, v196
	v_mov_b32_e32 v247, v197

.LBB0_929:
	s_lshl_b64 s[38:39], s[88:89], 13
	v_lshl_add_u64 v[102:103], v[214:215], 0, s[38:39]
	s_add_i32 m0, s34, 0x3000
	s_mul_i32 s34, s30, 0x5000
	global_load_lds_dwordx4 v[102:103], off
	s_add_i32 s34, s34, 0
	v_add_u32_e32 v224, s34, v231
	s_mul_i32 s35, s12, 0x5000
	s_mulk_i32 s33, 0x5000
	v_add_u32_e32 v235, s34, v233
	v_add_u32_e32 v210, s35, v232
	v_add_u32_e32 v225, s33, v234
	ds_read_b128 v[216:219], v224 offset:4608
	v_mfma_f32_32x32x16_bf16 v[114:129], v[240:243], v[130:133], 0
	v_exp_f32_e32 v82, v82
	v_exp_f32_e32 v83, v83
	v_exp_f32_e32 v84, v84
	v_mfma_f32_32x32x16_bf16 v[98:113], v[240:243], v[170:173], 0
	ds_read_b128 v[220:223], v224 offset:6656
	v_exp_f32_e32 v85, v85
	v_cvt_pk_bf16_f32 v198, v82, v83
	v_add_f32_e32 v212, v82, v212
	v_add_f32_e32 v212, v83, v212
	v_mfma_f32_32x32x16_bf16 v[114:129], v[244:247], v[134:137], v[114:129]
	v_exp_f32_e32 v86, v86
	v_exp_f32_e32 v87, v87
	v_cvt_pk_bf16_f32 v199, v84, v85
	v_add_f32_e32 v212, v84, v212
	v_mfma_f32_32x32x16_bf16 v[98:113], v[244:247], v[138:141], v[98:113]
	ds_read_b128 v[240:243], v224 offset:8704
	v_add_f32_e32 v212, v85, v212
	v_exp_f32_e32 v88, v88
	v_exp_f32_e32 v89, v89
	s_waitcnt lgkmcnt(2)
	v_mfma_f32_32x32x16_bf16 v[114:129], v[216:219], v[146:149], v[114:129]
	v_cvt_pk_bf16_f32 v200, v86, v87
	v_add_f32_e32 v212, v86, v212
	v_add_f32_e32 v212, v87, v212
	v_exp_f32_e32 v90, v90
	v_exp_f32_e32 v91, v91
	v_mfma_f32_32x32x16_bf16 v[98:113], v[216:219], v[142:145], v[98:113]
	ds_read_b128 v[244:247], v224 offset:10752
	v_cvt_pk_bf16_f32 v201, v88, v89
	v_add_f32_e32 v212, v88, v212
	v_add_f32_e32 v212, v89, v212
	v_exp_f32_e32 v92, v92
	s_waitcnt lgkmcnt(2)
	v_mfma_f32_32x32x16_bf16 v[114:129], v[220:223], v[150:153], v[114:129]
	v_exp_f32_e32 v93, v93
	v_cvt_pk_bf16_f32 v194, v90, v91
	v_add_f32_e32 v212, v90, v212
	v_add_f32_e32 v212, v91, v212
	v_mfma_f32_32x32x16_bf16 v[98:113], v[220:223], v[154:157], v[98:113]
	ds_read_b128 v[216:219], v225 offset:16384
	v_exp_f32_e32 v94, v94
	v_exp_f32_e32 v95, v95
	v_cvt_pk_bf16_f32 v195, v92, v93
	v_add_f32_e32 v212, v92, v212
	s_waitcnt lgkmcnt(2)
	v_mfma_f32_32x32x16_bf16 v[114:129], v[240:243], v[162:165], v[114:129]
	v_add_f32_e32 v212, v93, v212
	v_exp_f32_e32 v96, v96
	v_exp_f32_e32 v97, v97
	v_mfma_f32_32x32x16_bf16 v[98:113], v[240:243], v[158:161], v[98:113]
	ds_read_b128 v[220:223], v225 offset:16896
	v_cvt_pk_bf16_f32 v196, v94, v95
	v_add_f32_e32 v212, v94, v212
	v_add_f32_e32 v212, v95, v212
	v_exp_f32_e32 v66, v66
	v_exp_f32_e32 v67, v67
	s_waitcnt lgkmcnt(2)
	v_mfma_f32_32x32x16_bf16 v[114:129], v[244:247], v[166:169], v[114:129]
	v_cvt_pk_bf16_f32 v197, v96, v97
	v_add_f32_e32 v212, v96, v212
	v_add_f32_e32 v212, v97, v212
	v_exp_f32_e32 v68, v68
	v_mfma_f32_32x32x16_bf16 v[98:113], v[244:247], v[174:177], v[98:113]
	v_exp_f32_e32 v69, v69
	v_cvt_pk_bf16_f32 v202, v66, v67
	v_add_f32_e32 v213, v66, v213
	v_add_f32_e32 v213, v67, v213
	s_waitcnt lgkmcnt(1)
	v_mfma_f32_32x32x16_bf16 v[18:33], v[216:219], v[178:181], v[18:33]
	ds_read_b128 v[240:243], v225 offset:18432
	v_exp_f32_e32 v70, v70
	v_exp_f32_e32 v71, v71
	v_cvt_pk_bf16_f32 v203, v68, v69
	v_add_f32_e32 v213, v68, v213
	s_waitcnt lgkmcnt(1)
	v_mfma_f32_32x32x16_bf16 v[34:49], v[220:223], v[178:181], v[34:49]
	ds_read_b128 v[244:247], v225 offset:18944
	v_add_f32_e32 v213, v69, v213
	v_exp_f32_e32 v72, v72
	v_exp_f32_e32 v73, v73
	v_mfma_f32_32x32x16_bf16 v[50:65], v[216:219], v[190:193], v[50:65]
	v_cvt_pk_bf16_f32 v204, v70, v71
	v_add_f32_e32 v213, v70, v213
	v_add_f32_e32 v213, v71, v213
	v_exp_f32_e32 v74, v74
	v_exp_f32_e32 v75, v75
	v_mfma_f32_32x32x16_bf16 v[2:17], v[220:223], v[190:193], v[2:17]
	v_cvt_pk_bf16_f32 v205, v72, v73
	v_add_f32_e32 v213, v72, v213
	v_add_f32_e32 v213, v73, v213
	v_exp_f32_e32 v76, v76
	s_waitcnt lgkmcnt(1)
	v_mfma_f32_32x32x16_bf16 v[18:33], v[240:243], v[182:185], v[18:33]
	ds_read_b128 v[216:219], v210
	v_exp_f32_e32 v77, v77
	v_cvt_pk_bf16_f32 v206, v74, v75
	v_add_f32_e32 v213, v74, v213
	v_add_f32_e32 v213, v75, v213
	s_waitcnt lgkmcnt(1)
	v_mfma_f32_32x32x16_bf16 v[34:49], v[244:247], v[182:185], v[34:49]
	v_exp_f32_e32 v78, v78
	v_exp_f32_e32 v79, v79
	v_cvt_pk_bf16_f32 v207, v76, v77
	v_add_f32_e32 v213, v76, v213
	v_mfma_f32_32x32x16_bf16 v[50:65], v[240:243], v[186:189], v[50:65]
	ds_read_b128 v[220:223], v210 offset:2048
	v_add_f32_e32 v213, v77, v213
	v_exp_f32_e32 v80, v80
	v_exp_f32_e32 v81, v81
	v_mfma_f32_32x32x16_bf16 v[2:17], v[244:247], v[186:189], v[2:17]
	v_cvt_pk_bf16_f32 v208, v78, v79
	v_add_f32_e32 v213, v78, v213
	v_add_f32_e32 v213, v79, v213
	v_cvt_pk_bf16_f32 v209, v80, v81
	v_add_f32_e32 v213, v80, v213
	v_add_f32_e32 v213, v81, v213
	s_waitcnt lgkmcnt(1)
	v_mfma_f32_32x32x16_bf16 v[82:97], v[216:219], v[130:133], 0
	ds_read_b128 v[240:243], v210 offset:4096
	v_exp_f32_e32 v114, v114
	v_exp_f32_e32 v115, v115
	v_exp_f32_e32 v116, v116
	v_mfma_f32_32x32x16_bf16 v[66:81], v[216:219], v[170:173], 0
	v_exp_f32_e32 v117, v117
	v_cvt_pk_bf16_f32 v178, v114, v115
	v_add_f32_e32 v212, v114, v212
	v_add_f32_e32 v212, v115, v212
	s_waitcnt lgkmcnt(1)
	v_mfma_f32_32x32x16_bf16 v[82:97], v[220:223], v[134:137], v[82:97]
	ds_read_b128 v[244:247], v210 offset:6144
	v_exp_f32_e32 v118, v118
	v_exp_f32_e32 v119, v119
	v_cvt_pk_bf16_f32 v179, v116, v117
	v_add_f32_e32 v212, v116, v212
	v_mfma_f32_32x32x16_bf16 v[66:81], v[220:223], v[138:141], v[66:81]
	v_add_f32_e32 v212, v117, v212
	v_exp_f32_e32 v120, v120
	v_exp_f32_e32 v121, v121
	s_waitcnt lgkmcnt(1)
	v_mfma_f32_32x32x16_bf16 v[82:97], v[240:243], v[146:149], v[82:97]
	ds_read_b128 v[216:219], v210 offset:8192
	v_cvt_pk_bf16_f32 v180, v118, v119
	v_add_f32_e32 v212, v118, v212
	v_add_f32_e32 v212, v119, v212
	v_exp_f32_e32 v122, v122
	v_exp_f32_e32 v123, v123
	v_mfma_f32_32x32x16_bf16 v[66:81], v[240:243], v[142:145], v[66:81]
	v_cvt_pk_bf16_f32 v181, v120, v121
	v_add_f32_e32 v212, v120, v212
	v_add_f32_e32 v212, v121, v212
	v_exp_f32_e32 v124, v124
	s_waitcnt lgkmcnt(1)
	v_mfma_f32_32x32x16_bf16 v[82:97], v[244:247], v[150:153], v[82:97]
	ds_read_b128 v[220:223], v210 offset:10240
	v_exp_f32_e32 v125, v125
	v_cvt_pk_bf16_f32 v182, v122, v123
	v_add_f32_e32 v212, v122, v212
	v_add_f32_e32 v212, v123, v212
	v_mfma_f32_32x32x16_bf16 v[66:81], v[244:247], v[154:157], v[66:81]
	v_exp_f32_e32 v126, v126
	v_exp_f32_e32 v127, v127
	v_cvt_pk_bf16_f32 v183, v124, v125
	v_add_f32_e32 v212, v124, v212
	s_waitcnt lgkmcnt(1)
	v_mfma_f32_32x32x16_bf16 v[82:97], v[216:219], v[162:165], v[82:97]
	ds_read_b128 v[240:243], v235 offset:12288
	v_add_f32_e32 v212, v125, v212
	v_exp_f32_e32 v128, v128
	v_exp_f32_e32 v129, v129
	v_mfma_f32_32x32x16_bf16 v[66:81], v[216:219], v[158:161], v[66:81]
	ds_read_b128 v[244:247], v235 offset:12800
	v_cvt_pk_bf16_f32 v184, v126, v127
	v_add_f32_e32 v212, v126, v212
	v_add_f32_e32 v212, v127, v212
	v_exp_f32_e32 v98, v98
	v_exp_f32_e32 v99, v99
	s_waitcnt lgkmcnt(2)
	v_mfma_f32_32x32x16_bf16 v[82:97], v[220:223], v[166:169], v[82:97]
	v_cvt_pk_bf16_f32 v185, v128, v129
	v_add_f32_e32 v212, v128, v212
	v_add_f32_e32 v212, v129, v212
	v_exp_f32_e32 v100, v100
	v_mfma_f32_32x32x16_bf16 v[66:81], v[220:223], v[174:177], v[66:81]
	v_exp_f32_e32 v101, v101
	v_cvt_pk_bf16_f32 v190, v98, v99
	v_add_f32_e32 v213, v98, v213
	v_add_f32_e32 v213, v99, v213
	s_waitcnt lgkmcnt(1)
	v_mfma_f32_32x32x16_bf16 v[18:33], v[240:243], v[198:201], v[18:33]
	ds_read_b128 v[216:219], v235 offset:14336
	v_exp_f32_e32 v102, v102
	v_exp_f32_e32 v103, v103
	v_cvt_pk_bf16_f32 v191, v100, v101
	v_add_f32_e32 v213, v100, v213
	s_waitcnt lgkmcnt(1)
	v_mfma_f32_32x32x16_bf16 v[34:49], v[244:247], v[198:201], v[34:49]
	ds_read_b128 v[220:223], v235 offset:14848
	v_add_f32_e32 v213, v101, v213
	v_exp_f32_e32 v104, v104
	v_exp_f32_e32 v105, v105
	v_mfma_f32_32x32x16_bf16 v[50:65], v[240:243], v[202:205], v[50:65]
	v_cvt_pk_bf16_f32 v192, v102, v103
	v_add_f32_e32 v213, v102, v213
	v_add_f32_e32 v213, v103, v213
	v_exp_f32_e32 v106, v106
	v_exp_f32_e32 v107, v107
	v_mfma_f32_32x32x16_bf16 v[2:17], v[244:247], v[202:205], v[2:17]
	v_cvt_pk_bf16_f32 v193, v104, v105
	v_add_f32_e32 v213, v104, v213
	v_add_f32_e32 v213, v105, v213
	v_exp_f32_e32 v108, v108
	s_waitcnt lgkmcnt(1)
	v_mfma_f32_32x32x16_bf16 v[18:33], v[216:219], v[194:197], v[18:33]
	ds_read_b128 v[240:243], v210 offset:512
	v_exp_f32_e32 v109, v109
	v_cvt_pk_bf16_f32 v186, v106, v107
	v_add_f32_e32 v213, v106, v213
	v_add_f32_e32 v213, v107, v213
	s_waitcnt lgkmcnt(1)
	v_mfma_f32_32x32x16_bf16 v[34:49], v[220:223], v[194:197], v[34:49]
	v_exp_f32_e32 v110, v110
	v_exp_f32_e32 v111, v111
	v_cvt_pk_bf16_f32 v187, v108, v109
	v_add_f32_e32 v213, v108, v213
	v_mfma_f32_32x32x16_bf16 v[50:65], v[216:219], v[206:209], v[50:65]
	ds_read_b128 v[244:247], v210 offset:2560
	v_add_f32_e32 v213, v109, v213
	v_exp_f32_e32 v112, v112
	v_exp_f32_e32 v113, v113
	v_mfma_f32_32x32x16_bf16 v[2:17], v[220:223], v[206:209], v[2:17]
	v_cvt_pk_bf16_f32 v188, v110, v111
	v_add_f32_e32 v213, v110, v213
	v_add_f32_e32 v213, v111, v213
	v_cvt_pk_bf16_f32 v189, v112, v113
	v_add_f32_e32 v213, v112, v213
	v_add_f32_e32 v213, v113, v213
	s_add_i32 s33, s13, 1
	s_waitcnt vmcnt(0)
	s_and_b32 s34, s33, 3
	s_add_i32 s31, s31, 1
	s_cmpk_eq_i32 s31, 0x104
	s_waitcnt vmcnt(0) lgkmcnt(0)
	s_barrier
	s_cbranch_scc1 .LBB0_931
	s_mov_b32 s33, s30
	s_mov_b32 s30, s12
	s_mov_b32 s12, s13
	s_mov_b32 s13, s34
	s_branch .LBB0_927
